# nt on weight-conversion bf16 stores (9 conv loops); per_light 22/14; S5 epilogue hoist
# baseline (speedup 1.0000x reference)
; __device__ __forceinline__ u32x4 pack8(const float (&v)[8]) { u32x4 w; w.x = pk2(v[0], v[1]); w.y = pk2(v[2], v[3]); w.z = pk2(v[4], v[5]); w.w = pk2(v[6], v[7]); return w; }
; #define CV_JOB(i) conv_job(c, [&](int ii) { const int v = c.bid + (ii < mine ? ii : mine - 1) * G; return v < n0 ? lo0 + v : (v < n0 + n1 ? lo1 + (v - n0) : lo2 + (v - n0 - n1)); }(i))
; #define CV_ISSUE(i, buf) do { const ConvJob _j = CV_JOB(i); _Pragma("unroll") for (int _q = 0; _q < 8; ++_q) { const int _row = 2 * (_q * 8 + w) + lrow; const int _g = gp ^ cv_fz(_row); \
;         __builtin_amdgcn_global_load_lds((const unsigned*)(_j.src + (size_t)(_j.k0 + _row) * _j.ld + _j.col0 + _g * 4), (LAS unsigned*)(c.lds + (buf) * 65536 + (_q * 8 + w) * 1024), 16, 0, 2); } } while (0)
; __device__ __forceinline__ void conv_slice(const Ctx& c, int lo0, int n0, int lo1, int n1, int lo2, int n2) {
;     ...
;         u32x4 o[4];
; #pragma unroll
;         for (int p = 0; p < 2; ++p) { const int rr = rr0 + 64 * p, sc = (rr & ~31) + perm32(rr & 31), scg = sc >> 2, scl = sc & 3;
; #pragma unroll
;             for (int h = 0; h < 2; ++h) { float f[8];
; #pragma unroll
;                 for (int q = 0; q < 8; ++q) { const int k = 64 * h + kq * 8 + q; f[q] = B[k * 128 + ((scg ^ kq) << 2) + scl]; }
;                 o[p * 2 + h] = pack8(f); } }
;         asm volatile("s_waitcnt lgkmcnt(0)" ::: "memory");
;         __builtin_amdgcn_s_barrier();
;         asm volatile("" ::: "memory");
;         if ((i & 1) == 0) CV_ISSUE(i + 2, 0); else CV_ISSUE(i + 2, 1);
;         asm volatile("" ::: "memory");
;         { const ConvJob j = CV_JOB(i);
; #pragma unroll
;           for (int p = 0; p < 2; ++p) { bf16* d = j.dst + (size_t)(j.drow0 + rr0 + 64 * p) * j.dK + j.k0 + kq * 8;
; #pragma unroll
;               for (int h = 0; h < 2; ++h) *(u32x4*)(d + 64 * h) = o[p * 2 + h]; } }
.LBB0_90:
	s_ashr_i32 s11, s10, 31
	s_lshl_b64 s[10:11], s[10:11], 1
	v_add_u32_e32 v5, s18, v61
	s_add_u32 s10, s14, s10
	s_addc_u32 s11, s15, s11
	v_mov_b32_e32 v21, v3
	v_ashrrev_i32_e32 v7, 31, v5
	s_waitcnt lgkmcnt(0)
	v_cvt_pk_bf16_f32 v22, v22, v23
	v_cvt_pk_bf16_f32 v23, v24, v25
	v_cvt_pk_bf16_f32 v24, v26, v27
	v_cvt_pk_bf16_f32 v26, v30, v31
	v_cvt_pk_bf16_f32 v30, v38, v39
	v_cvt_pk_bf16_f32 v31, v40, v41
	v_lshl_add_u64 v[38:39], s[10:11], 0, v[20:21]
	v_mul_lo_u32 v7, s12, v7
	v_mul_lo_u32 v11, s13, v5
	v_mad_u64_u32 v[40:41], s[10:11], s12, v5, 0
	v_add3_u32 v41, v41, v7, v11
	v_add_u32_e32 v5, 64, v5
	v_cvt_pk_bf16_f32 v25, v28, v29
	v_lshl_add_u64 v[40:41], v[40:41], 1, v[38:39]
	v_ashrrev_i32_e32 v7, 31, v5
	v_cvt_pk_bf16_f32 v27, v32, v33
	v_cvt_pk_bf16_f32 v28, v34, v35
	v_cvt_pk_bf16_f32 v29, v36, v37
	global_store_dwordx4 v[40:41], v[22:25], off nt
	global_store_dwordx4 v[40:41], v[26:29], off offset:128 nt
	v_mul_lo_u32 v7, s12, v7
	v_mul_lo_u32 v11, s13, v5
	v_mad_u64_u32 v[22:23], s[10:11], s12, v5, 0
	v_add3_u32 v23, v23, v7, v11
	v_cvt_pk_bf16_f32 v32, v42, v43
	v_cvt_pk_bf16_f32 v33, v44, v45
	v_lshl_add_u64 v[22:23], v[22:23], 1, v[38:39]
	v_cvt_pk_bf16_f32 v34, v46, v47
	v_cvt_pk_bf16_f32 v35, v48, v49
	v_cvt_pk_bf16_f32 v36, v50, v51
	v_cvt_pk_bf16_f32 v37, v52, v53
	global_store_dwordx4 v[22:23], v[30:33], off nt
	global_store_dwordx4 v[22:23], v[34:37], off offset:128 nt
	s_add_i32 s77, s77, 1
	s_add_i32 s42, s42, s43
	s_add_i32 s44, s44, s45
	s_add_i32 s76, s76, s96
	s_cmp_eq_u32 s3, s77
	s_cbranch_scc1 .LBB0_153

; __device__ __forceinline__ u32x4 pack8(const float (&v)[8]) { u32x4 w; w.x = pk2(v[0], v[1]); w.y = pk2(v[2], v[3]); w.z = pk2(v[4], v[5]); w.w = pk2(v[6], v[7]); return w; }
; #define CV_JOB(i) conv_job(c, [&](int ii) { const int v = c.bid + (ii < mine ? ii : mine - 1) * G; return v < n0 ? lo0 + v : (v < n0 + n1 ? lo1 + (v - n0) : lo2 + (v - n0 - n1)); }(i))
; #define CV_ISSUE(i, buf) do { const ConvJob _j = CV_JOB(i); _Pragma("unroll") for (int _q = 0; _q < 8; ++_q) { const int _row = 2 * (_q * 8 + w) + lrow; const int _g = gp ^ cv_fz(_row); \
;         __builtin_amdgcn_global_load_lds((const unsigned*)(_j.src + (size_t)(_j.k0 + _row) * _j.ld + _j.col0 + _g * 4), (LAS unsigned*)(c.lds + (buf) * 65536 + (_q * 8 + w) * 1024), 16, 0, 2); } } while (0)
; __device__ __forceinline__ void conv_slice(const Ctx& c, int lo0, int n0, int lo1, int n1, int lo2, int n2) {
;     ...
;         u32x4 o[4];
; #pragma unroll
;         for (int p = 0; p < 2; ++p) { const int rr = rr0 + 64 * p, sc = (rr & ~31) + perm32(rr & 31), scg = sc >> 2, scl = sc & 3;
; #pragma unroll
;             for (int h = 0; h < 2; ++h) { float f[8];
; #pragma unroll
;                 for (int q = 0; q < 8; ++q) { const int k = 64 * h + kq * 8 + q; f[q] = B[k * 128 + ((scg ^ kq) << 2) + scl]; }
;                 o[p * 2 + h] = pack8(f); } }
;         asm volatile("s_waitcnt lgkmcnt(0)" ::: "memory");
;         __builtin_amdgcn_s_barrier();
;         asm volatile("" ::: "memory");
;         if ((i & 1) == 0) CV_ISSUE(i + 2, 0); else CV_ISSUE(i + 2, 1);
;         asm volatile("" ::: "memory");
;         { const ConvJob j = CV_JOB(i);
; #pragma unroll
;           for (int p = 0; p < 2; ++p) { bf16* d = j.dst + (size_t)(j.drow0 + rr0 + 64 * p) * j.dK + j.k0 + kq * 8;
; #pragma unroll
;               for (int h = 0; h < 2; ++h) *(u32x4*)(d + 64 * h) = o[p * 2 + h]; } }
.LBB0_310:
	s_ashr_i32 s17, s16, 31
	s_lshl_b64 s[16:17], s[16:17], 1
	v_add_u32_e32 v3, s24, v58
	s_add_u32 s16, s20, s16
	s_addc_u32 s17, s21, s17
	v_mov_b32_e32 v17, v1
	v_ashrrev_i32_e32 v5, 31, v3
	s_waitcnt lgkmcnt(0)
	v_cvt_pk_bf16_f32 v18, v18, v19
	v_cvt_pk_bf16_f32 v19, v20, v21
	v_cvt_pk_bf16_f32 v20, v22, v23
	v_cvt_pk_bf16_f32 v22, v26, v27
	v_cvt_pk_bf16_f32 v26, v34, v35
	v_cvt_pk_bf16_f32 v27, v36, v37
	v_lshl_add_u64 v[34:35], s[16:17], 0, v[16:17]
	v_mul_lo_u32 v5, s18, v5
	v_mul_lo_u32 v7, s19, v3
	v_mad_u64_u32 v[36:37], s[16:17], s18, v3, 0
	v_add3_u32 v37, v37, v5, v7
	v_add_u32_e32 v3, 64, v3
	v_cvt_pk_bf16_f32 v21, v24, v25
	v_lshl_add_u64 v[36:37], v[36:37], 1, v[34:35]
	v_ashrrev_i32_e32 v5, 31, v3
	v_cvt_pk_bf16_f32 v23, v28, v29
	v_cvt_pk_bf16_f32 v24, v30, v31
	v_cvt_pk_bf16_f32 v25, v32, v33
	global_store_dwordx4 v[36:37], v[18:21], off nt
	global_store_dwordx4 v[36:37], v[22:25], off offset:128 nt
	v_mul_lo_u32 v5, s18, v5
	v_mul_lo_u32 v7, s19, v3
	v_mad_u64_u32 v[18:19], s[16:17], s18, v3, 0
	v_add3_u32 v19, v19, v5, v7
	v_cvt_pk_bf16_f32 v28, v38, v39
	v_cvt_pk_bf16_f32 v29, v40, v41
	v_lshl_add_u64 v[18:19], v[18:19], 1, v[34:35]
	v_cvt_pk_bf16_f32 v30, v42, v43
	v_cvt_pk_bf16_f32 v31, v44, v45
	v_cvt_pk_bf16_f32 v32, v46, v47
	v_cvt_pk_bf16_f32 v33, v48, v49
	global_store_dwordx4 v[18:19], v[26:29], off nt
	global_store_dwordx4 v[18:19], v[30:33], off offset:128 nt
	s_add_i32 s85, s85, 1
	s_add_i32 s75, s75, s76
	s_add_i32 s77, s77, s78
	s_add_i32 s84, s84, s96
	s_cmp_eq_u32 s33, s85
	s_cbranch_scc1 .LBB0_373

; __device__ __forceinline__ u32x4 pack8(const float (&v)[8]) { u32x4 w; w.x = pk2(v[0], v[1]); w.y = pk2(v[2], v[3]); w.z = pk2(v[4], v[5]); w.w = pk2(v[6], v[7]); return w; }
; #define CV_JOB(i) conv_job(c, [&](int ii) { const int v = c.bid + (ii < mine ? ii : mine - 1) * G; return v < n0 ? lo0 + v : (v < n0 + n1 ? lo1 + (v - n0) : lo2 + (v - n0 - n1)); }(i))
; #define CV_ISSUE(i, buf) do { const ConvJob _j = CV_JOB(i); _Pragma("unroll") for (int _q = 0; _q < 8; ++_q) { const int _row = 2 * (_q * 8 + w) + lrow; const int _g = gp ^ cv_fz(_row); \
;         __builtin_amdgcn_global_load_lds((const unsigned*)(_j.src + (size_t)(_j.k0 + _row) * _j.ld + _j.col0 + _g * 4), (LAS unsigned*)(c.lds + (buf) * 65536 + (_q * 8 + w) * 1024), 16, 0, 2); } } while (0)
; __device__ __forceinline__ void conv_slice(const Ctx& c, int lo0, int n0, int lo1, int n1, int lo2, int n2) {
;     ...
;         u32x4 o[4];
; #pragma unroll
;         for (int p = 0; p < 2; ++p) { const int rr = rr0 + 64 * p, sc = (rr & ~31) + perm32(rr & 31), scg = sc >> 2, scl = sc & 3;
; #pragma unroll
;             for (int h = 0; h < 2; ++h) { float f[8];
; #pragma unroll
;                 for (int q = 0; q < 8; ++q) { const int k = 64 * h + kq * 8 + q; f[q] = B[k * 128 + ((scg ^ kq) << 2) + scl]; }
;                 o[p * 2 + h] = pack8(f); } }
;         asm volatile("s_waitcnt lgkmcnt(0)" ::: "memory");
;         __builtin_amdgcn_s_barrier();
;         asm volatile("" ::: "memory");
;         if ((i & 1) == 0) CV_ISSUE(i + 2, 0); else CV_ISSUE(i + 2, 1);
;         asm volatile("" ::: "memory");
;         { const ConvJob j = CV_JOB(i);
; #pragma unroll
;           for (int p = 0; p < 2; ++p) { bf16* d = j.dst + (size_t)(j.drow0 + rr0 + 64 * p) * j.dK + j.k0 + kq * 8;
; #pragma unroll
;               for (int h = 0; h < 2; ++h) *(u32x4*)(d + 64 * h) = o[p * 2 + h]; } }
.LBB0_895:
	s_ashr_i32 s21, s20, 31
	s_lshl_b64 s[20:21], s[20:21], 1
	v_add_u32_e32 v3, s28, v58
	s_add_u32 s20, s24, s20
	s_addc_u32 s21, s25, s21
	v_mov_b32_e32 v17, v1
	v_ashrrev_i32_e32 v5, 31, v3
	s_waitcnt lgkmcnt(0)
	v_cvt_pk_bf16_f32 v18, v18, v19
	v_cvt_pk_bf16_f32 v19, v20, v21
	v_cvt_pk_bf16_f32 v20, v22, v23
	v_cvt_pk_bf16_f32 v22, v26, v27
	v_cvt_pk_bf16_f32 v26, v34, v35
	v_cvt_pk_bf16_f32 v27, v36, v37
	v_lshl_add_u64 v[34:35], s[20:21], 0, v[16:17]
	v_mul_lo_u32 v5, s22, v5
	v_mul_lo_u32 v7, s23, v3
	v_mad_u64_u32 v[36:37], s[20:21], s22, v3, 0
	v_add3_u32 v37, v37, v5, v7
	v_add_u32_e32 v3, 64, v3
	v_cvt_pk_bf16_f32 v21, v24, v25
	v_lshl_add_u64 v[36:37], v[36:37], 1, v[34:35]
	v_ashrrev_i32_e32 v5, 31, v3
	v_cvt_pk_bf16_f32 v23, v28, v29
	v_cvt_pk_bf16_f32 v24, v30, v31
	v_cvt_pk_bf16_f32 v25, v32, v33
	global_store_dwordx4 v[36:37], v[18:21], off nt
	global_store_dwordx4 v[36:37], v[22:25], off offset:128 nt
	v_mul_lo_u32 v5, s22, v5
	v_mul_lo_u32 v7, s23, v3
	v_mad_u64_u32 v[18:19], s[20:21], s22, v3, 0
	v_add3_u32 v19, v19, v5, v7
	v_cvt_pk_bf16_f32 v28, v38, v39
	v_cvt_pk_bf16_f32 v29, v40, v41
	v_lshl_add_u64 v[18:19], v[18:19], 1, v[34:35]
	v_cvt_pk_bf16_f32 v30, v42, v43
	v_cvt_pk_bf16_f32 v31, v44, v45
	v_cvt_pk_bf16_f32 v32, v46, v47
	v_cvt_pk_bf16_f32 v33, v48, v49
	global_store_dwordx4 v[18:19], v[26:29], off nt
	global_store_dwordx4 v[18:19], v[30:33], off offset:128 nt
	s_add_i32 s84, s84, 1
	s_add_i32 s36, s36, s35
	s_cmp_eq_u32 s37, s84
	s_cbranch_scc1 .LBB0_958

; __device__ __forceinline__ u32x4 pack8(const float (&v)[8]) { u32x4 w; w.x = pk2(v[0], v[1]); w.y = pk2(v[2], v[3]); w.z = pk2(v[4], v[5]); w.w = pk2(v[6], v[7]); return w; }
; #define CV_JOB(i) conv_job(c, [&](int ii) { const int v = c.bid + (ii < mine ? ii : mine - 1) * G; return v < n0 ? lo0 + v : (v < n0 + n1 ? lo1 + (v - n0) : lo2 + (v - n0 - n1)); }(i))
; #define CV_ISSUE(i, buf) do { const ConvJob _j = CV_JOB(i); _Pragma("unroll") for (int _q = 0; _q < 8; ++_q) { const int _row = 2 * (_q * 8 + w) + lrow; const int _g = gp ^ cv_fz(_row); \
;         __builtin_amdgcn_global_load_lds((const unsigned*)(_j.src + (size_t)(_j.k0 + _row) * _j.ld + _j.col0 + _g * 4), (LAS unsigned*)(c.lds + (buf) * 65536 + (_q * 8 + w) * 1024), 16, 0, 2); } } while (0)
; __device__ __forceinline__ void conv_slice(const Ctx& c, int lo0, int n0, int lo1, int n1, int lo2, int n2) {
;     ...
;         u32x4 o[4];
; #pragma unroll
;         for (int p = 0; p < 2; ++p) { const int rr = rr0 + 64 * p, sc = (rr & ~31) + perm32(rr & 31), scg = sc >> 2, scl = sc & 3;
; #pragma unroll
;             for (int h = 0; h < 2; ++h) { float f[8];
; #pragma unroll
;                 for (int q = 0; q < 8; ++q) { const int k = 64 * h + kq * 8 + q; f[q] = B[k * 128 + ((scg ^ kq) << 2) + scl]; }
;                 o[p * 2 + h] = pack8(f); } }
;         asm volatile("s_waitcnt lgkmcnt(0)" ::: "memory");
;         __builtin_amdgcn_s_barrier();
;         asm volatile("" ::: "memory");
;         if ((i & 1) == 0) CV_ISSUE(i + 2, 0); else CV_ISSUE(i + 2, 1);
;         asm volatile("" ::: "memory");
;         { const ConvJob j = CV_JOB(i);
; #pragma unroll
;           for (int p = 0; p < 2; ++p) { bf16* d = j.dst + (size_t)(j.drow0 + rr0 + 64 * p) * j.dK + j.k0 + kq * 8;
; #pragma unroll
;               for (int h = 0; h < 2; ++h) *(u32x4*)(d + 64 * h) = o[p * 2 + h]; } }
.LBB0_997:
	s_ashr_i32 s21, s20, 31
	s_lshl_b64 s[20:21], s[20:21], 1
	v_add_u32_e32 v3, s28, v58
	s_add_u32 s20, s24, s20
	s_addc_u32 s21, s25, s21
	v_mov_b32_e32 v17, v1
	v_ashrrev_i32_e32 v5, 31, v3
	s_waitcnt lgkmcnt(0)
	v_cvt_pk_bf16_f32 v18, v18, v19
	v_cvt_pk_bf16_f32 v19, v20, v21
	v_cvt_pk_bf16_f32 v20, v22, v23
	v_cvt_pk_bf16_f32 v22, v26, v27
	v_cvt_pk_bf16_f32 v26, v34, v35
	v_cvt_pk_bf16_f32 v27, v36, v37
	v_lshl_add_u64 v[34:35], s[20:21], 0, v[16:17]
	v_mul_lo_u32 v5, s22, v5
	v_mul_lo_u32 v7, s23, v3
	v_mad_u64_u32 v[36:37], s[20:21], s22, v3, 0
	v_add3_u32 v37, v37, v5, v7
	v_add_u32_e32 v3, 64, v3
	v_cvt_pk_bf16_f32 v21, v24, v25
	v_lshl_add_u64 v[36:37], v[36:37], 1, v[34:35]
	v_ashrrev_i32_e32 v5, 31, v3
	v_cvt_pk_bf16_f32 v23, v28, v29
	v_cvt_pk_bf16_f32 v24, v30, v31
	v_cvt_pk_bf16_f32 v25, v32, v33
	global_store_dwordx4 v[36:37], v[18:21], off nt
	global_store_dwordx4 v[36:37], v[22:25], off offset:128 nt
	v_mul_lo_u32 v5, s22, v5
	v_mul_lo_u32 v7, s23, v3
	v_mad_u64_u32 v[18:19], s[20:21], s22, v3, 0
	v_add3_u32 v19, v19, v5, v7
	v_cvt_pk_bf16_f32 v28, v38, v39
	v_cvt_pk_bf16_f32 v29, v40, v41
	v_lshl_add_u64 v[18:19], v[18:19], 1, v[34:35]
	v_cvt_pk_bf16_f32 v30, v42, v43
	v_cvt_pk_bf16_f32 v31, v44, v45
	v_cvt_pk_bf16_f32 v32, v46, v47
	v_cvt_pk_bf16_f32 v33, v48, v49
	global_store_dwordx4 v[18:19], v[26:29], off nt
	global_store_dwordx4 v[18:19], v[30:33], off offset:128 nt
	s_add_i32 s76, s76, 1
	s_add_i32 s75, s75, s96
	s_cmp_eq_u32 s30, s76
	s_cbranch_scc1 .LBB0_1060

; __device__ __forceinline__ u32x4 pack8(const float (&v)[8]) { u32x4 w; w.x = pk2(v[0], v[1]); w.y = pk2(v[2], v[3]); w.z = pk2(v[4], v[5]); w.w = pk2(v[6], v[7]); return w; }
; #define CV_JOB(i) conv_job(c, [&](int ii) { const int v = c.bid + (ii < mine ? ii : mine - 1) * G; return v < n0 ? lo0 + v : (v < n0 + n1 ? lo1 + (v - n0) : lo2 + (v - n0 - n1)); }(i))
; #define CV_ISSUE(i, buf) do { const ConvJob _j = CV_JOB(i); _Pragma("unroll") for (int _q = 0; _q < 8; ++_q) { const int _row = 2 * (_q * 8 + w) + lrow; const int _g = gp ^ cv_fz(_row); \
;         __builtin_amdgcn_global_load_lds((const unsigned*)(_j.src + (size_t)(_j.k0 + _row) * _j.ld + _j.col0 + _g * 4), (LAS unsigned*)(c.lds + (buf) * 65536 + (_q * 8 + w) * 1024), 16, 0, 2); } } while (0)
; __device__ __forceinline__ void conv_slice(const Ctx& c, int lo0, int n0, int lo1, int n1, int lo2, int n2) {
;     ...
;         u32x4 o[4];
; #pragma unroll
;         for (int p = 0; p < 2; ++p) { const int rr = rr0 + 64 * p, sc = (rr & ~31) + perm32(rr & 31), scg = sc >> 2, scl = sc & 3;
; #pragma unroll
;             for (int h = 0; h < 2; ++h) { float f[8];
; #pragma unroll
;                 for (int q = 0; q < 8; ++q) { const int k = 64 * h + kq * 8 + q; f[q] = B[k * 128 + ((scg ^ kq) << 2) + scl]; }
;                 o[p * 2 + h] = pack8(f); } }
;         asm volatile("s_waitcnt lgkmcnt(0)" ::: "memory");
;         __builtin_amdgcn_s_barrier();
;         asm volatile("" ::: "memory");
;         if ((i & 1) == 0) CV_ISSUE(i + 2, 0); else CV_ISSUE(i + 2, 1);
;         asm volatile("" ::: "memory");
;         { const ConvJob j = CV_JOB(i);
; #pragma unroll
;           for (int p = 0; p < 2; ++p) { bf16* d = j.dst + (size_t)(j.drow0 + rr0 + 64 * p) * j.dK + j.k0 + kq * 8;
; #pragma unroll
;               for (int h = 0; h < 2; ++h) *(u32x4*)(d + 64 * h) = o[p * 2 + h]; } }
.LBB0_1258:
	s_ashr_i32 s19, s18, 31
	s_lshl_b64 s[18:19], s[18:19], 1
	v_add_u32_e32 v3, s26, v58
	s_add_u32 s18, s22, s18
	s_addc_u32 s19, s23, s19
	v_mov_b32_e32 v17, v1
	v_ashrrev_i32_e32 v5, 31, v3
	s_waitcnt lgkmcnt(0)
	v_cvt_pk_bf16_f32 v18, v18, v19
	v_cvt_pk_bf16_f32 v19, v20, v21
	v_cvt_pk_bf16_f32 v20, v22, v23
	v_cvt_pk_bf16_f32 v22, v26, v27
	v_cvt_pk_bf16_f32 v26, v34, v35
	v_cvt_pk_bf16_f32 v27, v36, v37
	v_lshl_add_u64 v[34:35], s[18:19], 0, v[16:17]
	v_mul_lo_u32 v5, s20, v5
	v_mul_lo_u32 v7, s21, v3
	v_mad_u64_u32 v[36:37], s[18:19], s20, v3, 0
	v_add3_u32 v37, v37, v5, v7
	v_add_u32_e32 v3, 64, v3
	v_cvt_pk_bf16_f32 v21, v24, v25
	v_lshl_add_u64 v[36:37], v[36:37], 1, v[34:35]
	v_ashrrev_i32_e32 v5, 31, v3
	v_cvt_pk_bf16_f32 v23, v28, v29
	v_cvt_pk_bf16_f32 v24, v30, v31
	v_cvt_pk_bf16_f32 v25, v32, v33
	global_store_dwordx4 v[36:37], v[18:21], off nt
	global_store_dwordx4 v[36:37], v[22:25], off offset:128 nt
	v_mul_lo_u32 v5, s20, v5
	v_mul_lo_u32 v7, s21, v3
	v_mad_u64_u32 v[18:19], s[18:19], s20, v3, 0
	v_add3_u32 v19, v19, v5, v7
	v_cvt_pk_bf16_f32 v28, v38, v39
	v_cvt_pk_bf16_f32 v29, v40, v41
	v_lshl_add_u64 v[18:19], v[18:19], 1, v[34:35]
	v_cvt_pk_bf16_f32 v30, v42, v43
	v_cvt_pk_bf16_f32 v31, v44, v45
	v_cvt_pk_bf16_f32 v32, v46, v47
	v_cvt_pk_bf16_f32 v33, v48, v49
	global_store_dwordx4 v[18:19], v[26:29], off nt
	global_store_dwordx4 v[18:19], v[30:33], off offset:128 nt
	s_add_i32 s84, s84, 1
	s_add_i32 s79, s79, s44
	s_cmp_eq_u32 s48, s84
	s_cbranch_scc1 .LBB0_1321

; __device__ __forceinline__ u32x4 pack8(const float (&v)[8]) { u32x4 w; w.x = pk2(v[0], v[1]); w.y = pk2(v[2], v[3]); w.z = pk2(v[4], v[5]); w.w = pk2(v[6], v[7]); return w; }
; #define CV_JOB(i) conv_job(c, [&](int ii) { const int v = c.bid + (ii < mine ? ii : mine - 1) * G; return v < n0 ? lo0 + v : (v < n0 + n1 ? lo1 + (v - n0) : lo2 + (v - n0 - n1)); }(i))
; #define CV_ISSUE(i, buf) do { const ConvJob _j = CV_JOB(i); _Pragma("unroll") for (int _q = 0; _q < 8; ++_q) { const int _row = 2 * (_q * 8 + w) + lrow; const int _g = gp ^ cv_fz(_row); \
;         __builtin_amdgcn_global_load_lds((const unsigned*)(_j.src + (size_t)(_j.k0 + _row) * _j.ld + _j.col0 + _g * 4), (LAS unsigned*)(c.lds + (buf) * 65536 + (_q * 8 + w) * 1024), 16, 0, 2); } } while (0)
; __device__ __forceinline__ void conv_slice(const Ctx& c, int lo0, int n0, int lo1, int n1, int lo2, int n2) {
;     ...
;         u32x4 o[4];
; #pragma unroll
;         for (int p = 0; p < 2; ++p) { const int rr = rr0 + 64 * p, sc = (rr & ~31) + perm32(rr & 31), scg = sc >> 2, scl = sc & 3;
; #pragma unroll
;             for (int h = 0; h < 2; ++h) { float f[8];
; #pragma unroll
;                 for (int q = 0; q < 8; ++q) { const int k = 64 * h + kq * 8 + q; f[q] = B[k * 128 + ((scg ^ kq) << 2) + scl]; }
;                 o[p * 2 + h] = pack8(f); } }
;         asm volatile("s_waitcnt lgkmcnt(0)" ::: "memory");
;         __builtin_amdgcn_s_barrier();
;         asm volatile("" ::: "memory");
;         if ((i & 1) == 0) CV_ISSUE(i + 2, 0); else CV_ISSUE(i + 2, 1);
;         asm volatile("" ::: "memory");
;         { const ConvJob j = CV_JOB(i);
; #pragma unroll
;           for (int p = 0; p < 2; ++p) { bf16* d = j.dst + (size_t)(j.drow0 + rr0 + 64 * p) * j.dK + j.k0 + kq * 8;
; #pragma unroll
;               for (int h = 0; h < 2; ++h) *(u32x4*)(d + 64 * h) = o[p * 2 + h]; } }
.LBB0_1360:
	s_ashr_i32 s19, s18, 31
	s_lshl_b64 s[18:19], s[18:19], 1
	v_add_u32_e32 v3, s26, v58
	s_add_u32 s18, s22, s18
	s_addc_u32 s19, s23, s19
	v_mov_b32_e32 v17, v1
	v_ashrrev_i32_e32 v5, 31, v3
	s_waitcnt lgkmcnt(0)
	v_cvt_pk_bf16_f32 v18, v18, v19
	v_cvt_pk_bf16_f32 v19, v20, v21
	v_cvt_pk_bf16_f32 v20, v22, v23
	v_cvt_pk_bf16_f32 v22, v26, v27
	v_cvt_pk_bf16_f32 v26, v34, v35
	v_cvt_pk_bf16_f32 v27, v36, v37
	v_lshl_add_u64 v[34:35], s[18:19], 0, v[16:17]
	v_mul_lo_u32 v5, s20, v5
	v_mul_lo_u32 v7, s21, v3
	v_mad_u64_u32 v[36:37], s[18:19], s20, v3, 0
	v_add3_u32 v37, v37, v5, v7
	v_add_u32_e32 v3, 64, v3
	v_cvt_pk_bf16_f32 v21, v24, v25
	v_lshl_add_u64 v[36:37], v[36:37], 1, v[34:35]
	v_ashrrev_i32_e32 v5, 31, v3
	v_cvt_pk_bf16_f32 v23, v28, v29
	v_cvt_pk_bf16_f32 v24, v30, v31
	v_cvt_pk_bf16_f32 v25, v32, v33
	global_store_dwordx4 v[36:37], v[18:21], off nt
	global_store_dwordx4 v[36:37], v[22:25], off offset:128 nt
	v_mul_lo_u32 v5, s20, v5
	v_mul_lo_u32 v7, s21, v3
	v_mad_u64_u32 v[18:19], s[18:19], s20, v3, 0
	v_add3_u32 v19, v19, v5, v7
	v_cvt_pk_bf16_f32 v28, v38, v39
	v_cvt_pk_bf16_f32 v29, v40, v41
	v_lshl_add_u64 v[18:19], v[18:19], 1, v[34:35]
	v_cvt_pk_bf16_f32 v30, v42, v43
	v_cvt_pk_bf16_f32 v31, v44, v45
	v_cvt_pk_bf16_f32 v32, v46, v47
	v_cvt_pk_bf16_f32 v33, v48, v49
	global_store_dwordx4 v[18:19], v[26:29], off nt
	global_store_dwordx4 v[18:19], v[30:33], off offset:128 nt
	s_add_i32 s76, s76, 1
	s_add_i32 s75, s75, s96
	s_cmp_eq_u32 s33, s76
	s_cbranch_scc1 .LBB0_1423

; __device__ __forceinline__ u32x4 pack8(const float (&v)[8]) { u32x4 w; w.x = pk2(v[0], v[1]); w.y = pk2(v[2], v[3]); w.z = pk2(v[4], v[5]); w.w = pk2(v[6], v[7]); return w; }
; #define CV_JOB(i) conv_job(c, [&](int ii) { const int v = c.bid + (ii < mine ? ii : mine - 1) * G; return v < n0 ? lo0 + v : (v < n0 + n1 ? lo1 + (v - n0) : lo2 + (v - n0 - n1)); }(i))
; #define CV_ISSUE(i, buf) do { const ConvJob _j = CV_JOB(i); _Pragma("unroll") for (int _q = 0; _q < 8; ++_q) { const int _row = 2 * (_q * 8 + w) + lrow; const int _g = gp ^ cv_fz(_row); \
;         __builtin_amdgcn_global_load_lds((const unsigned*)(_j.src + (size_t)(_j.k0 + _row) * _j.ld + _j.col0 + _g * 4), (LAS unsigned*)(c.lds + (buf) * 65536 + (_q * 8 + w) * 1024), 16, 0, 2); } } while (0)
; __device__ __forceinline__ void conv_slice(const Ctx& c, int lo0, int n0, int lo1, int n1, int lo2, int n2) {
;     ...
;         u32x4 o[4];
; #pragma unroll
;         for (int p = 0; p < 2; ++p) { const int rr = rr0 + 64 * p, sc = (rr & ~31) + perm32(rr & 31), scg = sc >> 2, scl = sc & 3;
; #pragma unroll
;             for (int h = 0; h < 2; ++h) { float f[8];
; #pragma unroll
;                 for (int q = 0; q < 8; ++q) { const int k = 64 * h + kq * 8 + q; f[q] = B[k * 128 + ((scg ^ kq) << 2) + scl]; }
;                 o[p * 2 + h] = pack8(f); } }
;         asm volatile("s_waitcnt lgkmcnt(0)" ::: "memory");
;         __builtin_amdgcn_s_barrier();
;         asm volatile("" ::: "memory");
;         if ((i & 1) == 0) CV_ISSUE(i + 2, 0); else CV_ISSUE(i + 2, 1);
;         asm volatile("" ::: "memory");
;         { const ConvJob j = CV_JOB(i);
; #pragma unroll
;           for (int p = 0; p < 2; ++p) { bf16* d = j.dst + (size_t)(j.drow0 + rr0 + 64 * p) * j.dK + j.k0 + kq * 8;
; #pragma unroll
;               for (int h = 0; h < 2; ++h) *(u32x4*)(d + 64 * h) = o[p * 2 + h]; } }
.LBB0_1899:
	s_ashr_i32 s21, s20, 31
	s_lshl_b64 s[20:21], s[20:21], 1
	v_add_u32_e32 v3, s28, v58
	s_add_u32 s20, s24, s20
	s_addc_u32 s21, s25, s21
	v_mov_b32_e32 v17, v1
	v_ashrrev_i32_e32 v5, 31, v3
	s_waitcnt lgkmcnt(0)
	v_cvt_pk_bf16_f32 v18, v18, v19
	v_cvt_pk_bf16_f32 v19, v20, v21
	v_cvt_pk_bf16_f32 v20, v22, v23
	v_cvt_pk_bf16_f32 v22, v26, v27
	v_cvt_pk_bf16_f32 v26, v34, v35
	v_cvt_pk_bf16_f32 v27, v36, v37
	v_lshl_add_u64 v[34:35], s[20:21], 0, v[16:17]
	v_mul_lo_u32 v5, s22, v5
	v_mul_lo_u32 v7, s23, v3
	v_mad_u64_u32 v[36:37], s[20:21], s22, v3, 0
	v_add3_u32 v37, v37, v5, v7
	v_add_u32_e32 v3, 64, v3
	v_cvt_pk_bf16_f32 v21, v24, v25
	v_lshl_add_u64 v[36:37], v[36:37], 1, v[34:35]
	v_ashrrev_i32_e32 v5, 31, v3
	v_cvt_pk_bf16_f32 v23, v28, v29
	v_cvt_pk_bf16_f32 v24, v30, v31
	v_cvt_pk_bf16_f32 v25, v32, v33
	global_store_dwordx4 v[36:37], v[18:21], off nt
	global_store_dwordx4 v[36:37], v[22:25], off offset:128 nt
	v_mul_lo_u32 v5, s22, v5
	v_mul_lo_u32 v7, s23, v3
	v_mad_u64_u32 v[18:19], s[20:21], s22, v3, 0
	v_add3_u32 v19, v19, v5, v7
	v_cvt_pk_bf16_f32 v28, v38, v39
	v_cvt_pk_bf16_f32 v29, v40, v41
	v_lshl_add_u64 v[18:19], v[18:19], 1, v[34:35]
	v_cvt_pk_bf16_f32 v30, v42, v43
	v_cvt_pk_bf16_f32 v31, v44, v45
	v_cvt_pk_bf16_f32 v32, v46, v47
	v_cvt_pk_bf16_f32 v33, v48, v49
	global_store_dwordx4 v[18:19], v[26:29], off nt
	global_store_dwordx4 v[18:19], v[30:33], off offset:128 nt
	s_add_i32 s75, s75, 1
	s_add_i32 s69, s69, s70
	s_add_i32 s71, s71, s72
	s_add_i32 s74, s74, s96
	s_cmp_eq_u32 s33, s75
	s_cbranch_scc1 .LBB0_1962

; __device__ __forceinline__ u32x4 pack8(const float (&v)[8]) { u32x4 w; w.x = pk2(v[0], v[1]); w.y = pk2(v[2], v[3]); w.z = pk2(v[4], v[5]); w.w = pk2(v[6], v[7]); return w; }
; #define CV_JOB(i) conv_job(c, [&](int ii) { const int v = c.bid + (ii < mine ? ii : mine - 1) * G; return v < n0 ? lo0 + v : (v < n0 + n1 ? lo1 + (v - n0) : lo2 + (v - n0 - n1)); }(i))
; #define CV_ISSUE(i, buf) do { const ConvJob _j = CV_JOB(i); _Pragma("unroll") for (int _q = 0; _q < 8; ++_q) { const int _row = 2 * (_q * 8 + w) + lrow; const int _g = gp ^ cv_fz(_row); \
;         __builtin_amdgcn_global_load_lds((const unsigned*)(_j.src + (size_t)(_j.k0 + _row) * _j.ld + _j.col0 + _g * 4), (LAS unsigned*)(c.lds + (buf) * 65536 + (_q * 8 + w) * 1024), 16, 0, 2); } } while (0)
; __device__ __forceinline__ void conv_slice(const Ctx& c, int lo0, int n0, int lo1, int n1, int lo2, int n2) {
;     ...
;         u32x4 o[4];
; #pragma unroll
;         for (int p = 0; p < 2; ++p) { const int rr = rr0 + 64 * p, sc = (rr & ~31) + perm32(rr & 31), scg = sc >> 2, scl = sc & 3;
; #pragma unroll
;             for (int h = 0; h < 2; ++h) { float f[8];
; #pragma unroll
;                 for (int q = 0; q < 8; ++q) { const int k = 64 * h + kq * 8 + q; f[q] = B[k * 128 + ((scg ^ kq) << 2) + scl]; }
;                 o[p * 2 + h] = pack8(f); } }
;         asm volatile("s_waitcnt lgkmcnt(0)" ::: "memory");
;         __builtin_amdgcn_s_barrier();
;         asm volatile("" ::: "memory");
;         if ((i & 1) == 0) CV_ISSUE(i + 2, 0); else CV_ISSUE(i + 2, 1);
;         asm volatile("" ::: "memory");
;         { const ConvJob j = CV_JOB(i);
; #pragma unroll
;           for (int p = 0; p < 2; ++p) { bf16* d = j.dst + (size_t)(j.drow0 + rr0 + 64 * p) * j.dK + j.k0 + kq * 8;
; #pragma unroll
;               for (int h = 0; h < 2; ++h) *(u32x4*)(d + 64 * h) = o[p * 2 + h]; } }
.LBB0_2223:
	s_ashr_i32 s21, s20, 31
	s_lshl_b64 s[20:21], s[20:21], 1
	v_add_u32_e32 v3, s28, v58
	s_add_u32 s20, s24, s20
	s_addc_u32 s21, s25, s21
	v_mov_b32_e32 v17, v1
	v_ashrrev_i32_e32 v5, 31, v3
	s_waitcnt lgkmcnt(0)
	v_cvt_pk_bf16_f32 v18, v18, v19
	v_cvt_pk_bf16_f32 v19, v20, v21
	v_cvt_pk_bf16_f32 v20, v22, v23
	v_cvt_pk_bf16_f32 v22, v26, v27
	v_cvt_pk_bf16_f32 v26, v34, v35
	v_cvt_pk_bf16_f32 v27, v36, v37
	v_lshl_add_u64 v[34:35], s[20:21], 0, v[16:17]
	v_mul_lo_u32 v5, s22, v5
	v_mul_lo_u32 v7, s23, v3
	v_mad_u64_u32 v[36:37], s[20:21], s22, v3, 0
	v_add3_u32 v37, v37, v5, v7
	v_add_u32_e32 v3, 64, v3
	v_cvt_pk_bf16_f32 v21, v24, v25
	v_lshl_add_u64 v[36:37], v[36:37], 1, v[34:35]
	v_ashrrev_i32_e32 v5, 31, v3
	v_cvt_pk_bf16_f32 v23, v28, v29
	v_cvt_pk_bf16_f32 v24, v30, v31
	v_cvt_pk_bf16_f32 v25, v32, v33
	global_store_dwordx4 v[36:37], v[18:21], off nt
	global_store_dwordx4 v[36:37], v[22:25], off offset:128 nt
	v_mul_lo_u32 v5, s22, v5
	v_mul_lo_u32 v7, s23, v3
	v_mad_u64_u32 v[18:19], s[20:21], s22, v3, 0
	v_add3_u32 v19, v19, v5, v7
	v_cvt_pk_bf16_f32 v28, v38, v39
	v_cvt_pk_bf16_f32 v29, v40, v41
	v_lshl_add_u64 v[18:19], v[18:19], 1, v[34:35]
	v_cvt_pk_bf16_f32 v30, v42, v43
	v_cvt_pk_bf16_f32 v31, v44, v45
	v_cvt_pk_bf16_f32 v32, v46, v47
	v_cvt_pk_bf16_f32 v33, v48, v49
	global_store_dwordx4 v[18:19], v[26:29], off nt
	global_store_dwordx4 v[18:19], v[30:33], off offset:128 nt
	s_add_i32 s78, s78, 1
	s_add_i32 s77, s77, s35
	s_cmp_eq_u32 s37, s78
	s_cbranch_scc1 .LBB0_2286

; __device__ __forceinline__ u32x4 pack8(const float (&v)[8]) { u32x4 w; w.x = pk2(v[0], v[1]); w.y = pk2(v[2], v[3]); w.z = pk2(v[4], v[5]); w.w = pk2(v[6], v[7]); return w; }
; #define CV_JOB(i) conv_job(c, [&](int ii) { const int v = c.bid + (ii < mine ? ii : mine - 1) * G; return v < n0 ? lo0 + v : (v < n0 + n1 ? lo1 + (v - n0) : lo2 + (v - n0 - n1)); }(i))
; #define CV_ISSUE(i, buf) do { const ConvJob _j = CV_JOB(i); _Pragma("unroll") for (int _q = 0; _q < 8; ++_q) { const int _row = 2 * (_q * 8 + w) + lrow; const int _g = gp ^ cv_fz(_row); \
;         __builtin_amdgcn_global_load_lds((const unsigned*)(_j.src + (size_t)(_j.k0 + _row) * _j.ld + _j.col0 + _g * 4), (LAS unsigned*)(c.lds + (buf) * 65536 + (_q * 8 + w) * 1024), 16, 0, 2); } } while (0)
; __device__ __forceinline__ void conv_slice(const Ctx& c, int lo0, int n0, int lo1, int n1, int lo2, int n2) {
;     ...
;         u32x4 o[4];
; #pragma unroll
;         for (int p = 0; p < 2; ++p) { const int rr = rr0 + 64 * p, sc = (rr & ~31) + perm32(rr & 31), scg = sc >> 2, scl = sc & 3;
; #pragma unroll
;             for (int h = 0; h < 2; ++h) { float f[8];
; #pragma unroll
;                 for (int q = 0; q < 8; ++q) { const int k = 64 * h + kq * 8 + q; f[q] = B[k * 128 + ((scg ^ kq) << 2) + scl]; }
;                 o[p * 2 + h] = pack8(f); } }
;         asm volatile("s_waitcnt lgkmcnt(0)" ::: "memory");
;         __builtin_amdgcn_s_barrier();
;         asm volatile("" ::: "memory");
;         if ((i & 1) == 0) CV_ISSUE(i + 2, 0); else CV_ISSUE(i + 2, 1);
;         asm volatile("" ::: "memory");
;         { const ConvJob j = CV_JOB(i);
; #pragma unroll
;           for (int p = 0; p < 2; ++p) { bf16* d = j.dst + (size_t)(j.drow0 + rr0 + 64 * p) * j.dK + j.k0 + kq * 8;
; #pragma unroll
;               for (int h = 0; h < 2; ++h) *(u32x4*)(d + 64 * h) = o[p * 2 + h]; } }
.LBB0_2325:
	s_ashr_i32 s21, s20, 31
	s_lshl_b64 s[20:21], s[20:21], 1
	v_add_u32_e32 v3, s28, v58
	s_add_u32 s20, s24, s20
	s_addc_u32 s21, s25, s21
	v_mov_b32_e32 v17, v1
	v_ashrrev_i32_e32 v5, 31, v3
	s_waitcnt lgkmcnt(0)
	v_cvt_pk_bf16_f32 v18, v18, v19
	v_cvt_pk_bf16_f32 v19, v20, v21
	v_cvt_pk_bf16_f32 v20, v22, v23
	v_cvt_pk_bf16_f32 v22, v26, v27
	v_cvt_pk_bf16_f32 v26, v34, v35
	v_cvt_pk_bf16_f32 v27, v36, v37
	v_lshl_add_u64 v[34:35], s[20:21], 0, v[16:17]
	v_mul_lo_u32 v5, s22, v5
	v_mul_lo_u32 v7, s23, v3
	v_mad_u64_u32 v[36:37], s[20:21], s22, v3, 0
	v_add3_u32 v37, v37, v5, v7
	v_add_u32_e32 v3, 64, v3
	v_cvt_pk_bf16_f32 v21, v24, v25
	v_lshl_add_u64 v[36:37], v[36:37], 1, v[34:35]
	v_ashrrev_i32_e32 v5, 31, v3
	v_cvt_pk_bf16_f32 v23, v28, v29
	v_cvt_pk_bf16_f32 v24, v30, v31
	v_cvt_pk_bf16_f32 v25, v32, v33
	global_store_dwordx4 v[36:37], v[18:21], off nt
	global_store_dwordx4 v[36:37], v[22:25], off offset:128 nt
	v_mul_lo_u32 v5, s22, v5
	v_mul_lo_u32 v7, s23, v3
	v_mad_u64_u32 v[18:19], s[20:21], s22, v3, 0
	v_add3_u32 v19, v19, v5, v7
	v_cvt_pk_bf16_f32 v28, v38, v39
	v_cvt_pk_bf16_f32 v29, v40, v41
	v_lshl_add_u64 v[18:19], v[18:19], 1, v[34:35]
	v_cvt_pk_bf16_f32 v30, v42, v43
	v_cvt_pk_bf16_f32 v31, v44, v45
	v_cvt_pk_bf16_f32 v32, v46, v47
	v_cvt_pk_bf16_f32 v33, v48, v49
	global_store_dwordx4 v[18:19], v[26:29], off nt
	global_store_dwordx4 v[18:19], v[30:33], off offset:128 nt
	s_add_i32 s74, s74, 1
	s_add_i32 s73, s73, s96
	s_cmp_eq_u32 s30, s74
	s_cbranch_scc1 .LBB0_2388
